# MoE down and combine phases keep the up phase's CNTL / BLK0 tables in LDS instead of reloading the counts and recomputing the prefix
# baseline (speedup 1.0000x reference)
.LBB0_3346:
	s_andn2_b64 vcc, exec, s[0:1]
	s_cbranch_vccnz .LBB0_3489
	s_mov_b32 s0, s23
	s_add_i32 s14, s0, 0
	s_add_i32 s0, s14, 0x20450
	s_waitcnt lgkmcnt(0)
	v_mov_b32_e32 v0, s0
	v_mov_b32_e32 v2, v251
	ds_read_b64 v[0:1], v0
	s_add_i32 s0, s14, 0x2016c
	v_add_u32_e32 v129, s94, v2
	v_mov_b32_e32 v2, s0
	ds_read_b32 v2, v2
	v_mov_b32_e32 v3, s97
	s_add_i32 s0, s14, 0x20448
	s_mov_b32 s26, s91
	s_waitcnt lgkmcnt(0)
	v_readfirstlane_b32 s11, v1
	v_subrev_co_u32_e32 v2, vcc, 1, v2
	v_readfirstlane_b32 s10, v0
	s_nop 0
	v_cndmask_b32_e32 v2, v2, v3, vcc
	s_add_i32 s5, s14, 0x20250
	v_readfirstlane_b32 s4, v2
	v_mov_b32_e32 v2, s0
	ds_read_b64 v[2:3], v2
	s_mov_b64 vcc, 0
	s_and_saveexec_b64 s[0:1], vcc
	s_cbranch_execz .LBB0_3349
	s_lshl_b32 s22, s62, 11
	s_lshl_b64 s[2:3], s[22:23], 2
	s_add_u32 s2, s10, s2
	v_lshlrev_b32_e32 v0, 6, v129
	s_addc_u32 s3, s11, s3
	v_ashrrev_i32_e32 v1, 31, v0
	v_lshl_add_u64 v[0:1], v[0:1], 2, s[2:3]
	v_add_co_u32_e32 v0, vcc, 0x10000, v0
	s_nop 1
	v_addc_co_u32_e32 v1, vcc, 0, v1, vcc
	global_load_dword v0, v[0:1], off sc1
	v_lshl_add_u32 v1, v129, 2, s5
	s_waitcnt vmcnt(0)
	ds_write_b32 v1, v0
.LBB0_3349:
	s_or_b64 exec, exec, s[0:1]
	s_mov_b64 vcc, 0
	s_waitcnt vmcnt(0) lgkmcnt(0)
	s_barrier
	s_and_saveexec_b64 s[0:1], vcc
	s_cbranch_execz .LBB0_3415
	s_mov_b64 s[2:3], exec
	s_mov_b64 exec, -1
	v_min_u32_e32 v1, 31, v129
	v_lshl_add_u32 v1, v1, 2, s5
	ds_read_b32 v0, v1
	v_cmp_gt_u32_e32 vcc, 32, v129
	s_waitcnt lgkmcnt(0)
	v_add_u32_e32 v0, 0xff, v0
	v_ashrrev_i32_e32 v0, 8, v0
	v_cndmask_b32_e32 v0, 0, v0, vcc
	s_nop 1
	v_add_u32_dpp v2, v0, v0 row_shr:1 row_mask:0xf bank_mask:0xf bound_ctrl:1
	s_nop 1
	v_add_u32_dpp v2, v2, v2 row_shr:2 row_mask:0xf bank_mask:0xf bound_ctrl:1
	s_nop 1
	v_add_u32_dpp v2, v2, v2 row_shr:4 row_mask:0xf bank_mask:0xf bound_ctrl:1
	s_nop 1
	v_add_u32_dpp v2, v2, v2 row_shr:8 row_mask:0xf bank_mask:0xf bound_ctrl:1
	s_nop 1
	v_add_u32_dpp v2, v2, v2 row_bcast:15 row_mask:0xa bank_mask:0xf
	s_nop 1
	v_add_u32_dpp v2, v2, v2 row_bcast:31 row_mask:0xc bank_mask:0xf
	s_mov_b64 exec, s[2:3]
	v_sub_u32_e32 v0, v2, v0
	v_lshl_add_u32 v1, v129, 2, s14
	v_add_u32_e32 v1, 0x201c0, v1
	ds_write_b32 v1, v0
	s_add_i32 s5, s14, 0x202cc

.LBB0_3492:
	s_mov_b32 s0, s23
	s_add_i32 s8, s0, 0
	s_add_i32 s0, s8, 0x20450
	s_waitcnt lgkmcnt(0)
	v_mov_b32_e32 v0, s0
	v_mov_b32_e32 v2, v251
	ds_read_b64 v[0:1], v0
	s_add_i32 s0, s8, 0x2016c
	v_add_u32_e32 v126, s94, v2
	v_mov_b32_e32 v2, s0
	ds_read_b32 v2, v2
	v_mov_b32_e32 v3, s97
	s_add_i32 s0, s8, 0x20448
	s_mov_b32 s20, s91
	s_waitcnt lgkmcnt(0)
	v_readfirstlane_b32 s3, v1
	v_subrev_co_u32_e32 v2, vcc, 1, v2
	v_readfirstlane_b32 s2, v0
	s_nop 0
	v_cndmask_b32_e32 v2, v2, v3, vcc
	v_readfirstlane_b32 s10, v126
	v_readfirstlane_b32 s9, v2
	v_mov_b32_e32 v2, s0
	ds_read_b64 v[2:3], v2
	s_add_i32 s11, s8, 0x20250
	s_mov_b64 vcc, 0
	s_waitcnt lgkmcnt(0)
	v_readfirstlane_b32 s1, v3
	v_readfirstlane_b32 s0, v2
	s_and_saveexec_b64 s[4:5], vcc
	s_cbranch_execz .LBB0_3494
	s_lshl_b32 s22, s62, 11
	s_lshl_b64 s[6:7], s[22:23], 2
	s_add_u32 s6, s2, s6
	v_lshlrev_b32_e32 v0, 6, v126
	s_addc_u32 s7, s3, s7
	v_ashrrev_i32_e32 v1, 31, v0
	v_lshl_add_u64 v[0:1], v[0:1], 2, s[6:7]
	v_add_co_u32_e32 v0, vcc, 0x10000, v0
	s_nop 1
	v_addc_co_u32_e32 v1, vcc, 0, v1, vcc
	global_load_dword v0, v[0:1], off sc1
	v_lshl_add_u32 v1, v126, 2, s11
	s_waitcnt vmcnt(0)
	ds_write_b32 v1, v0
.LBB0_3494:
	s_or_b64 exec, exec, s[4:5]
	s_add_i32 s26, s8, 0x201c0
	s_mov_b64 vcc, 0
	s_waitcnt vmcnt(0) lgkmcnt(0)
	s_barrier
	s_and_saveexec_b64 s[4:5], vcc
	s_cbranch_execz .LBB0_3560
	s_mov_b64 s[6:7], exec
	s_mov_b64 exec, -1
	v_min_u32_e32 v1, 31, v126
	v_lshl_add_u32 v1, v1, 2, s11
	ds_read_b32 v0, v1
	v_cmp_gt_u32_e32 vcc, 32, v126
	s_waitcnt lgkmcnt(0)
	v_add_u32_e32 v0, 0xff, v0
	v_ashrrev_i32_e32 v0, 8, v0
	v_cndmask_b32_e32 v0, 0, v0, vcc
	s_nop 1
	v_add_u32_dpp v2, v0, v0 row_shr:1 row_mask:0xf bank_mask:0xf bound_ctrl:1
	s_nop 1
	v_add_u32_dpp v2, v2, v2 row_shr:2 row_mask:0xf bank_mask:0xf bound_ctrl:1
	s_nop 1
	v_add_u32_dpp v2, v2, v2 row_shr:4 row_mask:0xf bank_mask:0xf bound_ctrl:1
	s_nop 1
	v_add_u32_dpp v2, v2, v2 row_shr:8 row_mask:0xf bank_mask:0xf bound_ctrl:1
	s_nop 1
	v_add_u32_dpp v2, v2, v2 row_bcast:15 row_mask:0xa bank_mask:0xf
	s_nop 1
	v_add_u32_dpp v2, v2, v2 row_bcast:31 row_mask:0xc bank_mask:0xf
	s_mov_b64 exec, s[6:7]
	v_sub_u32_e32 v0, v2, v0
	v_lshl_add_u32 v1, v126, 2, s26
	ds_write_b32 v1, v0
	s_add_i32 s11, s8, 0x202cc
